# XCD-local barriers as v38, placement check also requires the 256-workgroup grid (same run-time path; second timing sample)
# baseline (speedup 1.0000x reference)
_Z6mk_fwd4Args:
	s_load_dword s10, s[0:1], 0x90
	s_mov_b32 s11, s2
	s_add_u32 s2, s0, 0x90
	s_addc_u32 s3, s1, 0
	v_lshl_add_u32 v1, v0, 2, 0
	v_writelane_b32 v253, s2, 0
	v_add_u32_e32 v1, 0x20000, v1
	v_mov_b32_e32 v2, 0
	v_readfirstlane_b32 s22, v0
	v_writelane_b32 v253, s3, 1
	ds_write2st64_b32 v1, v2, v2 offset1:8
	ds_write2st64_b32 v1, v2, v2 offset0:16 offset1:24
	v_or_b32_e32 v1, 0x800, v0
	s_mov_b64 s[2:3], -1
	s_and_saveexec_b64 s[4:5], s[2:3]
	v_lshl_add_u32 v3, v1, 2, 0
	v_add_u32_e32 v3, 0x20000, v3
	ds_write_b32 v3, v2
	s_or_b64 exec, exec, s[4:5]
	s_and_saveexec_b64 s[4:5], s[2:3]
	s_add_i32 s2, 0, 0x20000
	v_lshl_add_u32 v1, v1, 2, s2
	v_mov_b32_e32 v2, 0
	ds_write_b32 v1, v2 offset:2048
	s_or_b64 exec, exec, s[4:5]
	v_or_b32_e32 v1, 0xc00, v0
	v_cmp_gt_u32_e64 s[2:3], 7, 6
	v_cmp_gt_u32_e64 s[6:7], 7, 5
	s_and_saveexec_b64 s[4:5], s[6:7]
	v_lshl_add_u32 v2, v1, 2, 0
	v_add_u32_e32 v2, 0x20000, v2
	v_mov_b32_e32 v3, 0
	ds_write_b32 v2, v3
	s_or_b64 exec, exec, s[4:5]
	s_load_dwordx16 s[48:63], s[0:1], 0x40
	s_and_saveexec_b64 s[4:5], s[2:3]
	s_add_i32 s2, 0, 0x20000
	v_lshl_add_u32 v1, v1, 2, s2
	v_mov_b32_e32 v2, 0
	ds_write_b32 v1, v2 offset:2048
	s_or_b64 exec, exec, s[4:5]
	s_waitcnt lgkmcnt(0)
	s_add_u32 s2, s62, 0x4000
	s_addc_u32 s3, s63, 0
	v_writelane_b32 v253, s2, 2
	s_barrier
	s_nop 0
	v_writelane_b32 v253, s3, 3
	s_getreg_b32 s6, hwreg(HW_REG_XCC_ID, 0, 4)
	v_cmp_eq_u32_e64 s[4:5], 0, v0
	s_mov_b64 s[2:3], exec
	s_nop 0
	v_writelane_b32 v253, s4, 4
	s_nop 1
	v_writelane_b32 v253, s5, 5
	s_and_b64 s[4:5], s[2:3], s[4:5]
	s_mov_b64 exec, s[4:5]
	s_cbranch_execz .LBB0_11
	s_mov_b64 s[4:5], exec
	v_mbcnt_lo_u32_b32 v1, s4, 0
	v_mbcnt_hi_u32_b32 v1, s5, v1
	v_cmp_eq_u32_e32 vcc, 0, v1
	s_and_b64 s[8:9], exec, vcc
	s_mov_b64 exec, s[8:9]
	s_cbranch_execz .LBB0_11
	s_lshl_b32 s6, s6, 8
	s_bcnt1_i32_b64 s4, s[4:5]
	s_and_b32 s6, s6, 0xf00
	v_mov_b32_e32 v2, s4
	v_readlane_b32 s4, v253, 2
	v_mov_b32_e32 v1, s6
	v_readlane_b32 s5, v253, 3
	s_nop 4
	global_atomic_add v1, v2, s[4:5] offset:1024
	s_lshr_b32 s6, s6, 8
	s_and_b32 s7, s11, 7
	s_cmp_eq_u32 s6, s7
	s_cbranch_scc0 .Lmm_bad
	s_cmpk_eq_i32 s10, 0x100
	s_cbranch_scc1 .Lmm_ok
.Lmm_bad:
	v_mov_b32_e32 v1, 0x300
	s_nop 0
	global_atomic_add v1, v2, s[4:5]
